# P4 gain hoist, compiler's wait ladder over the row loads kept
# baseline (speedup 1.0000x reference)
; DI unsigned pk2(float lo, float hi) { return cvtpk_s(lo, hi); }
; DI void p4_store(const P4Row& R, const float* hg, bf16_t* YC, int row, int lane) {
; #pragma unroll
;     for (int j = 0; j < 4; ++j) {
;         const int c0 = 512 * j + 8 * lane; const u32x4 o = R.o[j], sg = R.sg[j];
;         float v[8] = {bflo(o.x), bfhi(o.x), bflo(o.y), bfhi(o.y), bflo(o.z), bfhi(o.z), bflo(o.w), bfhi(o.w)};
;         const float s[8] = {bflo(sg.x), bfhi(sg.x), bflo(sg.y), bfhi(sg.y), bflo(sg.z), bfhi(sg.z), bflo(sg.w), bfhi(sg.w)};
;         float ss = 0.f;
; #pragma unroll
;         for (int e = 0; e < 8; ++e) ss += v[e] * v[e];
;         ss += __shfl_xor(ss, 1); ss += __shfl_xor(ss, 2); ss += __shfl_xor(ss, 4); ss += __shfl_xor(ss, 8);
;         const float rinv = rsqrtf(ss * (1.0f / 128.0f) + EPS);
;         const f32x4 g0 = *(const f32x4*)(hg + c0), g1 = *(const f32x4*)(hg + c0 + 4);
; #pragma unroll
;         for (int e = 0; e < 4; ++e) { v[e] = v[e] * rinv * g0[e] * s[e]; v[4 + e] = v[4 + e] * rinv * g1[e] * s[4 + e]; }
;         u32x4 w; w.x = pk2(v[0], v[1]); w.y = pk2(v[2], v[3]); w.z = pk2(v[4], v[5]); w.w = pk2(v[6], v[7]);
;         *(u32x4*)(YC + (size_t)row * KCAT + 512 + c0) = w;
;     }
.LBB0_530:
	s_nop 0
	s_waitcnt vmcnt(13)
	v_and_b32_e32 v143, 0xffff0000, v86
	s_waitcnt vmcnt(12)
	v_and_b32_e32 v153, 0xffff0000, v82
	v_lshlrev_b32_e32 v138, 16, v87
	v_and_b32_e32 v139, 0xffff0000, v87
	v_lshlrev_b32_e32 v142, 16, v86
	v_lshlrev_b32_e32 v148, 16, v83
	v_and_b32_e32 v149, 0xffff0000, v83
	v_lshlrev_b32_e32 v152, 16, v82
	v_mov_b32_e32 v154, v153
	v_mov_b32_e32 v155, v143
	v_pk_mul_f32 v[140:141], v[138:139], v[138:139]
	v_pk_mul_f32 v[150:151], v[148:149], v[148:149]
	v_mov_b32_e32 v82, v152
	v_mov_b32_e32 v83, v142
	v_pk_mul_f32 v[154:155], v[154:155], v[154:155]
	v_lshlrev_b32_e32 v136, 16, v88
	v_and_b32_e32 v137, 0xffff0000, v88
	v_lshlrev_b32_e32 v146, 16, v84
	v_and_b32_e32 v147, 0xffff0000, v84
	v_pk_fma_f32 v[82:83], v[82:83], v[82:83], v[154:155]
	v_mov_b32_e32 v154, v150
	v_mov_b32_e32 v155, v140
	v_lshlrev_b32_e32 v116, 16, v89
	v_and_b32_e32 v117, 0xffff0000, v89
	v_pk_mul_f32 v[88:89], v[136:137], v[136:137]
	v_lshlrev_b32_e32 v144, 16, v85
	v_and_b32_e32 v145, 0xffff0000, v85
	v_pk_mul_f32 v[84:85], v[146:147], v[146:147]
	v_pk_add_f32 v[82:83], v[154:155], v[82:83]
	v_mov_b32_e32 v140, v151
	v_pk_add_f32 v[82:83], v[140:141], v[82:83]
	v_mov_b32_e32 v140, v84
	v_mov_b32_e32 v141, v88
	v_pk_mul_f32 v[134:135], v[116:117], v[116:117]
	v_pk_mul_f32 v[86:87], v[144:145], v[144:145]
	v_pk_add_f32 v[82:83], v[140:141], v[82:83]
	v_mov_b32_e32 v88, v85
	v_pk_add_f32 v[82:83], v[88:89], v[82:83]
	v_mov_b32_e32 v84, v86
	v_mov_b32_e32 v85, v134
	v_pk_add_f32 v[82:83], v[84:85], v[82:83]
	v_mov_b32_e32 v134, v87
	v_pk_add_f32 v[82:83], v[134:135], v[82:83]
	ds_bpermute_b32 v85, v1, v83
	ds_bpermute_b32 v84, v1, v82
	s_waitcnt vmcnt(11)
	v_lshlrev_b32_e32 v86, 16, v81
	v_and_b32_e32 v87, 0xffff0000, v81
	v_lshlrev_b32_e32 v88, 16, v80
	v_and_b32_e32 v89, 0xffff0000, v80
	s_waitcnt lgkmcnt(0)
	v_pk_add_f32 v[82:83], v[82:83], v[84:85]
	ds_bpermute_b32 v85, v118, v83
	ds_bpermute_b32 v84, v118, v82
	v_lshlrev_b32_e32 v140, 16, v79
	v_and_b32_e32 v141, 0xffff0000, v79
	s_waitcnt vmcnt(3)
	v_max3_f32 v129, v126, v127, v128
	s_waitcnt lgkmcnt(0)
	v_pk_add_f32 v[82:83], v[82:83], v[84:85]
	ds_bpermute_b32 v85, v119, v83
	ds_bpermute_b32 v84, v119, v82
	s_waitcnt lgkmcnt(0)
	v_pk_add_f32 v[84:85], v[82:83], v[84:85]
	ds_bpermute_b32 v135, v120, v85
	ds_bpermute_b32 v134, v120, v84
	v_mov_b64_e32 v[82:83], s[22:23]
	s_waitcnt lgkmcnt(0)
	v_pk_add_f32 v[80:81], v[84:85], v[134:135]
	s_nop 0
	v_pk_fma_f32 v[150:151], v[80:81], s[20:21], v[82:83] op_sel_hi:[1,0,0]
	v_lshlrev_b32_e32 v84, 16, v78
	v_mul_f32_e32 v79, 0x4b800000, v151
	v_cmp_gt_f32_e32 vcc, s29, v151
	v_and_b32_e32 v85, 0xffff0000, v78
	v_lshl_add_u64 v[80:81], s[8:9], 0, v[104:105]
	v_cndmask_b32_e32 v79, v151, v79, vcc
	v_rsq_f32_e32 v79, v79
	s_nop 0
	v_mul_f32_e32 v78, 0x45800000, v79
	v_cndmask_b32_e32 v78, v79, v78, vcc
	v_pk_mul_f32 v[134:135], v[78:79], v[142:143] op_sel_hi:[0,1]
	v_pk_mul_f32 v[136:137], v[78:79], v[136:137] op_sel_hi:[0,1]
	v_pk_mul_f32 v[138:139], v[78:79], v[138:139] op_sel_hi:[0,1]
	v_pk_mul_f32 v[78:79], v[78:79], v[116:117] op_sel_hi:[0,1]
	v_pk_mul_f32 v[78:79], v[162:163], v[78:79]
	s_waitcnt vmcnt(0)
	v_pk_mul_f32 v[130:131], v[164:165], v[134:135]
	v_pk_mul_f32 v[112:113], v[160:161], v[136:137]
	v_pk_mul_f32 v[132:133], v[166:167], v[138:139]
	v_pk_mul_f32 v[78:79], v[78:79], v[86:87]
	v_pk_mul_f32 v[84:85], v[130:131], v[84:85]
	v_pk_mul_f32 v[88:89], v[112:113], v[88:89]
	v_pk_mul_f32 v[112:113], v[132:133], v[140:141]
	v_cvt_pk_bf16_f32 v87, v78, v79
	v_add_co_u32_e32 v78, vcc, s30, v80
	v_cvt_pk_bf16_f32 v84, v84, v85
	v_cvt_pk_bf16_f32 v85, v112, v113
	v_cvt_pk_bf16_f32 v86, v88, v89
	v_addc_co_u32_e32 v79, vcc, 0, v81, vcc
	global_store_dwordx4 v[78:79], v[84:87], off offset:1024
	s_nop 1
	v_lshlrev_b32_e32 v86, 16, v65
	v_and_b32_e32 v87, 0xffff0000, v65
	v_mul_f32_e32 v65, 0x4b800000, v150
	v_cmp_gt_f32_e32 vcc, s29, v150
	v_lshlrev_b32_e32 v116, 16, v71
	v_and_b32_e32 v117, 0xffff0000, v71
	v_cndmask_b32_e32 v65, v150, v65, vcc
	v_rsq_f32_e32 v65, v65
	v_lshlrev_b32_e32 v114, 16, v72
	v_and_b32_e32 v115, 0xffff0000, v72
	v_lshlrev_b32_e32 v84, 16, v77
	v_mul_f32_e32 v71, 0x45800000, v65
	v_cndmask_b32_e32 v72, v65, v71, vcc
	v_and_b32_e32 v85, 0xffff0000, v77
	v_lshlrev_b32_e32 v138, 16, v76
	v_and_b32_e32 v139, 0xffff0000, v76
	v_lshlrev_b32_e32 v76, 16, v75
	v_and_b32_e32 v77, 0xffff0000, v75
	v_lshlrev_b32_e32 v140, 16, v74
	v_and_b32_e32 v141, 0xffff0000, v74
	v_lshlrev_b32_e32 v88, 16, v73
	v_and_b32_e32 v89, 0xffff0000, v73
	v_pk_mul_f32 v[74:75], v[72:73], v[152:153] op_sel_hi:[0,1]
	v_pk_mul_f32 v[142:143], v[72:73], v[146:147] op_sel_hi:[0,1]
	v_pk_mul_f32 v[146:147], v[72:73], v[148:149] op_sel_hi:[0,1]
	v_pk_mul_f32 v[72:73], v[72:73], v[144:145] op_sel_hi:[0,1]
	v_and_b32_e32 v71, 0xffff0000, v69
	v_lshlrev_b32_e32 v112, 16, v64
	v_and_b32_e32 v113, 0xffff0000, v64
	v_lshlrev_b32_e32 v64, 16, v60
	v_and_b32_e32 v65, 0xffff0000, v60
	v_lshlrev_b32_e32 v60, 16, v59
	v_pk_mul_f32 v[74:75], v[168:169], v[74:75]
	v_pk_mul_f32 v[130:131], v[172:173], v[142:143]
	v_pk_mul_f32 v[132:133], v[170:171], v[146:147]
	v_pk_mul_f32 v[72:73], v[174:175], v[72:73]
	v_pk_mul_f32 v[74:75], v[74:75], v[140:141]
	v_pk_mul_f32 v[130:131], v[130:131], v[138:139]
	v_pk_mul_f32 v[76:77], v[132:133], v[76:77]
	v_pk_mul_f32 v[84:85], v[72:73], v[84:85]
	v_cvt_pk_bf16_f32 v72, v74, v75
	v_cvt_pk_bf16_f32 v73, v76, v77
	v_cvt_pk_bf16_f32 v74, v130, v131
	v_cvt_pk_bf16_f32 v75, v84, v85
	global_store_dwordx4 v[78:79], v[72:75], off offset:2048
	s_nop 0
	v_and_b32_e32 v135, 0xffff0000, v70
	v_and_b32_e32 v85, 0xffff0000, v66
; DI unsigned pk2(float lo, float hi) { return cvtpk_s(lo, hi); }
; DI void p4_store(const P4Row& R, const float* hg, bf16_t* YC, int row, int lane) {
; #pragma unroll
;     for (int j = 0; j < 4; ++j) {
;         const int c0 = 512 * j + 8 * lane; const u32x4 o = R.o[j], sg = R.sg[j];
;         float v[8] = {bflo(o.x), bfhi(o.x), bflo(o.y), bfhi(o.y), bflo(o.z), bfhi(o.z), bflo(o.w), bfhi(o.w)};
;         const float s[8] = {bflo(sg.x), bfhi(sg.x), bflo(sg.y), bfhi(sg.y), bflo(sg.z), bfhi(sg.z), bflo(sg.w), bfhi(sg.w)};
;         float ss = 0.f;
; #pragma unroll
;         for (int e = 0; e < 8; ++e) ss += v[e] * v[e];
;         ss += __shfl_xor(ss, 1); ss += __shfl_xor(ss, 2); ss += __shfl_xor(ss, 4); ss += __shfl_xor(ss, 8);
;         const float rinv = rsqrtf(ss * (1.0f / 128.0f) + EPS);
;         const f32x4 g0 = *(const f32x4*)(hg + c0), g1 = *(const f32x4*)(hg + c0 + 4);
; #pragma unroll
;         for (int e = 0; e < 4; ++e) { v[e] = v[e] * rinv * g0[e] * s[e]; v[4 + e] = v[4 + e] * rinv * g1[e] * s[4 + e]; }
;         u32x4 w; w.x = pk2(v[0], v[1]); w.y = pk2(v[2], v[3]); w.z = pk2(v[4], v[5]); w.w = pk2(v[6], v[7]);
;         *(u32x4*)(YC + (size_t)row * KCAT + 512 + c0) = w;
;     }
;     {
;         const int c0 = 8 * lane; const float l0 = R.l0, l1 = R.l1, l2 = R.l2; const u32x4 x0 = R.x0, x1 = R.x1, x2 = R.x2;
;         const float mx = fmaxf(l0, fmaxf(l1, l2)); float a0 = __expf(l0 - mx), a1 = __expf(l1 - mx), a2 = __expf(l2 - mx);
;         const float inv = 1.0f / (a0 + a1 + a2); a0 *= inv; a1 *= inv; a2 *= inv;
;         u32x4 w;
;         w.x = pk2(a0 * bflo(x0.x) + a1 * bflo(x1.x) + a2 * bflo(x2.x), a0 * bfhi(x0.x) + a1 * bfhi(x1.x) + a2 * bfhi(x2.x));
;         w.y = pk2(a0 * bflo(x0.y) + a1 * bflo(x1.y) + a2 * bflo(x2.y), a0 * bfhi(x0.y) + a1 * bfhi(x1.y) + a2 * bfhi(x2.y));
;         w.z = pk2(a0 * bflo(x0.z) + a1 * bflo(x1.z) + a2 * bflo(x2.z), a0 * bfhi(x0.z) + a1 * bfhi(x1.z) + a2 * bfhi(x2.z));
;         w.w = pk2(a0 * bflo(x0.w) + a1 * bflo(x1.w) + a2 * bflo(x2.w), a0 * bfhi(x0.w) + a1 * bfhi(x1.w) + a2 * bfhi(x2.w));
;         *(u32x4*)(YC + (size_t)row * KCAT + c0) = w;
;     }
; }
	v_lshlrev_b32_e32 v134, 16, v70
	v_lshlrev_b32_e32 v70, 16, v69
	v_lshlrev_b32_e32 v76, 16, v68
	v_and_b32_e32 v77, 0xffff0000, v68
	v_lshlrev_b32_e32 v68, 16, v67
	v_and_b32_e32 v69, 0xffff0000, v67
	v_lshlrev_b32_e32 v84, 16, v66
	v_mov_b32_e32 v148, v85
	v_mov_b32_e32 v149, v135
	v_pk_mul_f32 v[66:67], v[88:89], v[88:89]
	v_pk_mul_f32 v[136:137], v[114:115], v[114:115]
	v_pk_mul_f32 v[138:139], v[116:117], v[116:117]
	v_pk_mul_f32 v[140:141], v[70:71], v[70:71]
	v_pk_mul_f32 v[142:143], v[76:77], v[76:77]
	v_pk_mul_f32 v[144:145], v[68:69], v[68:69]
	v_mov_b32_e32 v146, v84
	v_mov_b32_e32 v147, v134
	v_pk_mul_f32 v[148:149], v[148:149], v[148:149]
	v_mov_b32_e32 v150, v144
	v_mov_b32_e32 v151, v138
	v_mov_b32_e32 v138, v145
	v_mov_b32_e32 v144, v142
	v_mov_b32_e32 v145, v136
	v_mov_b32_e32 v136, v143
	v_mov_b32_e32 v142, v140
	v_mov_b32_e32 v143, v66
	v_mov_b32_e32 v66, v141
	v_pk_fma_f32 v[140:141], v[146:147], v[146:147], v[148:149]
	s_nop 0
	v_pk_add_f32 v[140:141], v[150:151], v[140:141]
	s_nop 0
	v_pk_add_f32 v[138:139], v[138:139], v[140:141]
	v_lshlrev_b32_e32 v140, 16, v62
	v_pk_add_f32 v[138:139], v[144:145], v[138:139]
	v_and_b32_e32 v141, 0xffff0000, v62
	v_pk_add_f32 v[136:137], v[136:137], v[138:139]
	v_lshlrev_b32_e32 v138, 16, v63
	v_pk_add_f32 v[136:137], v[142:143], v[136:137]
	v_and_b32_e32 v139, 0xffff0000, v63
	v_pk_add_f32 v[66:67], v[66:67], v[136:137]
	ds_bpermute_b32 v137, v1, v67
	ds_bpermute_b32 v136, v1, v66
	v_lshlrev_b32_e32 v62, 16, v61
	v_and_b32_e32 v63, 0xffff0000, v61
	v_and_b32_e32 v61, 0xffff0000, v59
	v_and_b32_e32 v59, 0xffff0000, v46
	s_waitcnt lgkmcnt(0)
	v_pk_add_f32 v[66:67], v[66:67], v[136:137]
	ds_bpermute_b32 v137, v118, v67
	ds_bpermute_b32 v136, v118, v66
	s_waitcnt lgkmcnt(0)
	v_pk_add_f32 v[136:137], v[66:67], v[136:137]
	ds_bpermute_b32 v143, v119, v137
	ds_bpermute_b32 v142, v119, v136
	v_lshlrev_b32_e32 v66, 16, v58
	v_and_b32_e32 v67, 0xffff0000, v58
	v_lshlrev_b32_e32 v58, 16, v54
	s_waitcnt lgkmcnt(0)
	v_pk_add_f32 v[136:137], v[136:137], v[142:143]
	ds_bpermute_b32 v143, v120, v137
	ds_bpermute_b32 v142, v120, v136
	s_waitcnt lgkmcnt(0)
	v_pk_add_f32 v[136:137], v[136:137], v[142:143]
	s_nop 0
	v_pk_fma_f32 v[82:83], v[136:137], s[20:21], v[82:83] op_sel_hi:[1,0,0]
	v_and_b32_e32 v137, 0xffff0000, v54
	v_mul_f32_e32 v136, 0x4b800000, v83
	v_cmp_gt_f32_e32 vcc, s29, v83
	v_lshlrev_b32_e32 v54, 16, v56
	v_lshlrev_b32_e32 v142, 16, v50
	v_cndmask_b32_e32 v83, v83, v136, vcc
	v_rsq_f32_e32 v83, v83
	v_lshlrev_b32_e32 v136, 16, v46
	v_and_b32_e32 v143, 0xffff0000, v50
	v_lshlrev_b32_e32 v50, 16, v51
	v_mul_f32_e32 v46, 0x45800000, v83
	v_cndmask_b32_e32 v46, v83, v46, vcc
	v_pk_mul_f32 v[134:135], v[46:47], v[134:135] op_sel_hi:[0,1]
	v_pk_mul_f32 v[114:115], v[46:47], v[114:115] op_sel_hi:[0,1]
	v_pk_mul_f32 v[116:117], v[46:47], v[116:117] op_sel_hi:[0,1]
	v_pk_mul_f32 v[88:89], v[46:47], v[88:89] op_sel_hi:[0,1]
	v_pk_mul_f32 v[130:131], v[180:181], v[134:135]
	v_pk_mul_f32 v[72:73], v[176:177], v[114:115]
	v_pk_mul_f32 v[114:115], v[182:183], v[116:117]
	v_pk_mul_f32 v[74:75], v[178:179], v[88:89]
	v_pk_mul_f32 v[88:89], v[130:131], v[140:141]
	v_pk_mul_f32 v[112:113], v[72:73], v[112:113]
	v_pk_mul_f32 v[114:115], v[114:115], v[138:139]
	v_pk_mul_f32 v[86:87], v[74:75], v[86:87]
	v_cvt_pk_bf16_f32 v72, v88, v89
	v_cvt_pk_bf16_f32 v73, v114, v115
	v_cvt_pk_bf16_f32 v74, v112, v113
	v_cvt_pk_bf16_f32 v75, v86, v87
	global_store_dwordx4 v[78:79], v[72:75], off offset:3072
	s_nop 0
	v_lshlrev_b32_e32 v112, 16, v55
	v_and_b32_e32 v113, 0xffff0000, v47
	v_lshlrev_b32_e32 v46, 16, v47
	v_and_b32_e32 v47, 0xffff0000, v55
	v_and_b32_e32 v55, 0xffff0000, v48
	v_lshlrev_b32_e32 v114, 16, v48
	v_and_b32_e32 v115, 0xffff0000, v56
	v_lshlrev_b32_e32 v130, 16, v57
	v_and_b32_e32 v131, 0xffff0000, v49
	v_lshlrev_b32_e32 v48, 16, v49
	v_and_b32_e32 v49, 0xffff0000, v57
	v_sub_f32_e32 v56, v126, v129
	v_sub_f32_e32 v57, v127, v129
	v_sub_f32_e32 v83, v128, v129
	v_mul_f32_e32 v56, 0x3fb8aa3b, v56
	v_mul_f32_e32 v126, 0x3fb8aa3b, v57
	v_mul_f32_e32 v83, 0x3fb8aa3b, v83
	v_exp_f32_e32 v57, v56
	v_exp_f32_e32 v56, v126
	v_exp_f32_e32 v83, v83
	v_add_co_u32_e32 v80, vcc, s31, v80
	v_add_f32_e32 v126, v57, v56
	v_add_f32_e32 v126, v83, v126
	v_div_scale_f32 v127, s[34:35], v126, v126, 1.0
	v_rcp_f32_e32 v128, v127
	v_addc_co_u32_e32 v81, vcc, 0, v81, vcc
	v_div_scale_f32 v129, vcc, 1.0, v126, 1.0
	v_fma_f32 v132, -v127, v128, 1.0
	v_fmac_f32_e32 v128, v132, v128
	v_mul_f32_e32 v132, v129, v128
	v_fma_f32 v133, -v127, v132, v129
	v_fmac_f32_e32 v132, v133, v128
	v_fma_f32 v127, -v127, v132, v129
	v_div_fmas_f32 v127, v127, v128, v132
	v_div_fixup_f32 v126, v127, v126, 1.0
	v_pk_mul_f32 v[56:57], v[56:57], v[126:127] op_sel_hi:[1,0]
	v_and_b32_e32 v51, 0xffff0000, v51
	v_pk_mul_f32 v[46:47], v[56:57], v[46:47] op_sel:[1,0] op_sel_hi:[0,1]
	v_mul_f32_e32 v128, v83, v126
	v_pk_mul_f32 v[126:127], v[56:57], v[136:137] op_sel:[1,0] op_sel_hi:[0,1]
	v_pk_fma_f32 v[46:47], v[56:57], v[112:113], v[46:47]
	s_andn2_b64 vcc, exec, s[4:5]
	v_pk_mul_f32 v[114:115], v[56:57], v[114:115] op_sel:[1,0] op_sel_hi:[0,1]
	v_pk_mul_f32 v[48:49], v[56:57], v[48:49] op_sel:[1,0] op_sel_hi:[0,1]
	v_pk_fma_f32 v[58:59], v[56:57], v[58:59], v[126:127]
	v_pk_fma_f32 v[50:51], v[128:129], v[50:51], v[46:47] op_sel_hi:[0,1,1]
	v_mul_f32_e32 v47, 0x4b800000, v82
	v_cmp_gt_f32_e64 s[4:5], s29, v82
	v_pk_fma_f32 v[54:55], v[56:57], v[54:55], v[114:115]
	v_pk_fma_f32 v[48:49], v[56:57], v[130:131], v[48:49]
	v_pk_fma_f32 v[56:57], v[128:129], v[142:143], v[58:59] op_sel_hi:[0,1,1]
	v_cndmask_b32_e64 v47, v82, v47, s[4:5]
	v_cvt_pk_bf16_f32 v46, v56, v57
	v_rsq_f32_e32 v56, v47
	v_lshlrev_b32_e32 v116, 16, v52
	v_and_b32_e32 v117, 0xffff0000, v52
	v_lshlrev_b32_e32 v52, 16, v53
	v_and_b32_e32 v53, 0xffff0000, v53
	v_cvt_pk_bf16_f32 v47, v50, v51
	v_mul_f32_e32 v50, 0x45800000, v56
	v_pk_fma_f32 v[54:55], v[128:129], v[116:117], v[54:55] op_sel_hi:[0,1,1]
	v_pk_fma_f32 v[52:53], v[128:129], v[52:53], v[48:49] op_sel_hi:[0,1,1]
	v_cndmask_b32_e64 v50, v56, v50, s[4:5]
	v_cvt_pk_bf16_f32 v48, v54, v55
	v_cvt_pk_bf16_f32 v49, v52, v53
	v_pk_mul_f32 v[52:53], v[50:51], v[84:85] op_sel_hi:[0,1]
	v_pk_mul_f32 v[54:55], v[50:51], v[76:77] op_sel_hi:[0,1]
	v_pk_mul_f32 v[56:57], v[50:51], v[68:69] op_sel_hi:[0,1]
	v_pk_mul_f32 v[50:51], v[50:51], v[70:71] op_sel_hi:[0,1]
	v_pk_mul_f32 v[54:55], v[184:185], v[54:55]
	v_pk_mul_f32 v[52:53], v[188:189], v[52:53]
	v_pk_mul_f32 v[56:57], v[190:191], v[56:57]
	v_pk_mul_f32 v[50:51], v[186:187], v[50:51]
	v_pk_mul_f32 v[52:53], v[52:53], v[66:67]
	v_pk_mul_f32 v[54:55], v[54:55], v[64:65]
	v_pk_mul_f32 v[56:57], v[56:57], v[60:61]
	v_pk_mul_f32 v[58:59], v[50:51], v[62:63]
	v_cvt_pk_bf16_f32 v50, v52, v53
	v_cvt_pk_bf16_f32 v51, v56, v57
	v_cvt_pk_bf16_f32 v52, v54, v55
	v_cvt_pk_bf16_f32 v53, v58, v59
	global_store_dwordx4 v[80:81], v[50:53], off
	global_store_dwordx4 v[78:79], v[46:49], off
	s_cbranch_vccnz .LBB0_527
; DI unsigned pk2(float lo, float hi) { return cvtpk_s(lo, hi); }
; DI void p4_store(const P4Row& R, const float* hg, bf16_t* YC, int row, int lane) {
; #pragma unroll
;     for (int j = 0; j < 4; ++j) {
;         const int c0 = 512 * j + 8 * lane; const u32x4 o = R.o[j], sg = R.sg[j];
;         float v[8] = {bflo(o.x), bfhi(o.x), bflo(o.y), bfhi(o.y), bflo(o.z), bfhi(o.z), bflo(o.w), bfhi(o.w)};
;         const float s[8] = {bflo(sg.x), bfhi(sg.x), bflo(sg.y), bfhi(sg.y), bflo(sg.z), bfhi(sg.z), bflo(sg.w), bfhi(sg.w)};
;         float ss = 0.f;
; #pragma unroll
;         for (int e = 0; e < 8; ++e) ss += v[e] * v[e];
;         ss += __shfl_xor(ss, 1); ss += __shfl_xor(ss, 2); ss += __shfl_xor(ss, 4); ss += __shfl_xor(ss, 8);
;         const float rinv = rsqrtf(ss * (1.0f / 128.0f) + EPS);
;         const f32x4 g0 = *(const f32x4*)(hg + c0), g1 = *(const f32x4*)(hg + c0 + 4);
; #pragma unroll
;         for (int e = 0; e < 4; ++e) { v[e] = v[e] * rinv * g0[e] * s[e]; v[4 + e] = v[4 + e] * rinv * g1[e] * s[4 + e]; }
;         u32x4 w; w.x = pk2(v[0], v[1]); w.y = pk2(v[2], v[3]); w.z = pk2(v[4], v[5]); w.w = pk2(v[6], v[7]);
;         *(u32x4*)(YC + (size_t)row * KCAT + 512 + c0) = w;
;     }
	v_and_b32_e32 v67, 0xffff0000, v2
	v_and_b32_e32 v81, 0xffff0000, v6
	v_lshlrev_b32_e32 v62, 16, v3
	v_and_b32_e32 v63, 0xffff0000, v3
	v_lshlrev_b32_e32 v66, 16, v2
	v_lshlrev_b32_e32 v76, 16, v7
	v_and_b32_e32 v77, 0xffff0000, v7
	v_lshlrev_b32_e32 v80, 16, v6
	v_mov_b32_e32 v84, v81
	v_mov_b32_e32 v85, v67
	v_pk_mul_f32 v[64:65], v[62:63], v[62:63]
	v_pk_mul_f32 v[78:79], v[76:77], v[76:77]
	v_mov_b32_e32 v82, v80
	v_mov_b32_e32 v83, v66
	v_pk_mul_f32 v[84:85], v[84:85], v[84:85]
	v_lshlrev_b32_e32 v58, 16, v4
	v_and_b32_e32 v59, 0xffff0000, v4
	v_lshlrev_b32_e32 v72, 16, v8
	v_and_b32_e32 v73, 0xffff0000, v8
	v_pk_fma_f32 v[82:83], v[82:83], v[82:83], v[84:85]
	v_mov_b32_e32 v84, v78
	v_mov_b32_e32 v85, v64
	v_pk_mul_f32 v[60:61], v[58:59], v[58:59]
	v_pk_mul_f32 v[74:75], v[72:73], v[72:73]
	v_pk_add_f32 v[82:83], v[84:85], v[82:83]
	v_mov_b32_e32 v64, v79
	v_lshlrev_b32_e32 v54, 16, v5
	v_and_b32_e32 v55, 0xffff0000, v5
	v_lshlrev_b32_e32 v68, 16, v9
	v_and_b32_e32 v69, 0xffff0000, v9
	v_pk_add_f32 v[64:65], v[64:65], v[82:83]
	v_mov_b32_e32 v78, v74
	v_mov_b32_e32 v79, v60
	v_pk_mul_f32 v[56:57], v[54:55], v[54:55]
	v_pk_mul_f32 v[70:71], v[68:69], v[68:69]
	v_pk_add_f32 v[64:65], v[78:79], v[64:65]
	v_mov_b32_e32 v60, v75
	v_pk_add_f32 v[60:61], v[60:61], v[64:65]
	v_mov_b32_e32 v64, v70
	v_mov_b32_e32 v65, v56
	v_pk_add_f32 v[60:61], v[64:65], v[60:61]
	v_mov_b32_e32 v56, v71
	v_pk_add_f32 v[56:57], v[56:57], v[60:61]
	ds_bpermute_b32 v61, v1, v57
	ds_bpermute_b32 v60, v1, v56
	v_mov_b64_e32 v[82:83], s[22:23]
	v_lshlrev_b32_e32 v70, 16, v16
	v_and_b32_e32 v71, 0xffff0000, v16
	v_lshlrev_b32_e32 v74, 16, v15
	s_waitcnt lgkmcnt(0)
	v_pk_add_f32 v[56:57], v[56:57], v[60:61]
	ds_bpermute_b32 v61, v118, v57
	ds_bpermute_b32 v60, v118, v56
	v_and_b32_e32 v75, 0xffff0000, v15
	s_mul_i32 s4, s24, 0x1400
	v_lshlrev_b32_e32 v64, 16, v17
	v_and_b32_e32 v65, 0xffff0000, v17
	s_waitcnt lgkmcnt(0)
	v_pk_add_f32 v[56:57], v[56:57], v[60:61]
	ds_bpermute_b32 v61, v119, v57
	ds_bpermute_b32 v60, v119, v56
	v_lshlrev_b32_e32 v78, 16, v14
	v_and_b32_e32 v79, 0xffff0000, v14
	s_mul_hi_i32 s5, s24, 0x1400
	s_add_u32 s4, s3, s4
	s_waitcnt lgkmcnt(0)
	v_pk_add_f32 v[56:57], v[56:57], v[60:61]
	ds_bpermute_b32 v61, v120, v57
	ds_bpermute_b32 v60, v120, v56
	s_addc_u32 s5, s21, s5
	v_lshlrev_b32_e32 v114, 16, v37
	v_lshlrev_b32_e32 v112, 16, v41
	v_and_b32_e32 v113, 0xffff0000, v37
	s_waitcnt lgkmcnt(0)
	v_pk_add_f32 v[56:57], v[56:57], v[60:61]
	v_lshlrev_b32_e32 v126, 16, v45
	v_pk_fma_f32 v[56:57], v[56:57], s[20:21], v[82:83] op_sel_hi:[1,0,0]
	s_nop 0
	v_mul_f32_e32 v60, 0x4b800000, v57
	v_cmp_gt_f32_e32 vcc, s29, v57
	s_nop 1
	v_cndmask_b32_e32 v57, v57, v60, vcc
	v_rsq_f32_e32 v57, v57
	s_nop 0
	v_mul_f32_e32 v60, 0x45800000, v57
	v_cndmask_b32_e32 v60, v57, v60, vcc
	v_pk_mul_f32 v[58:59], v[60:61], v[58:59] op_sel_hi:[0,1]
	v_pk_mul_f32 v[46:47], v[160:161], v[58:59]
	v_pk_mul_f32 v[66:67], v[60:61], v[66:67] op_sel_hi:[0,1]
	v_pk_mul_f32 v[58:59], v[46:47], v[70:71]
	v_pk_mul_f32 v[46:47], v[60:61], v[62:63] op_sel_hi:[0,1]
	v_pk_mul_f32 v[46:47], v[166:167], v[46:47]
	v_pk_mul_f32 v[50:51], v[164:165], v[66:67]
	v_pk_mul_f32 v[52:53], v[46:47], v[74:75]
	v_pk_mul_f32 v[46:47], v[60:61], v[54:55] op_sel_hi:[0,1]
	v_pk_mul_f32 v[46:47], v[162:163], v[46:47]
	v_pk_mul_f32 v[50:51], v[50:51], v[78:79]
	v_pk_mul_f32 v[54:55], v[46:47], v[64:65]
	v_cvt_pk_bf16_f32 v46, v50, v51
	v_cvt_pk_bf16_f32 v47, v52, v53
	v_cvt_pk_bf16_f32 v48, v58, v59
	v_cvt_pk_bf16_f32 v49, v54, v55
	global_store_dwordx4 v121, v[46:49], s[4:5] offset:1024
	s_nop 0
	v_mul_f32_e32 v57, 0x4b800000, v56
	v_cmp_gt_f32_e32 vcc, s29, v56
	v_lshlrev_b32_e32 v54, 16, v21
	v_and_b32_e32 v55, 0xffff0000, v21
	v_cndmask_b32_e32 v56, v56, v57, vcc
	v_rsq_f32_e32 v56, v56
	v_lshlrev_b32_e32 v58, 16, v20
	v_and_b32_e32 v59, 0xffff0000, v20
	v_lshlrev_b32_e32 v60, 16, v19
	v_mul_f32_e32 v57, 0x45800000, v56
	v_cndmask_b32_e32 v56, v56, v57, vcc
	v_pk_mul_f32 v[74:75], v[56:57], v[80:81] op_sel_hi:[0,1]
	v_pk_mul_f32 v[72:73], v[56:57], v[72:73] op_sel_hi:[0,1]
	v_pk_mul_f32 v[76:77], v[56:57], v[76:77] op_sel_hi:[0,1]
	v_pk_mul_f32 v[56:57], v[56:57], v[68:69] op_sel_hi:[0,1]
	v_and_b32_e32 v61, 0xffff0000, v19
	v_lshlrev_b32_e32 v62, 16, v18
	v_and_b32_e32 v63, 0xffff0000, v18
	v_lshlrev_b32_e32 v64, 16, v13
	v_and_b32_e32 v65, 0xffff0000, v13
	v_lshlrev_b32_e32 v66, 16, v12
	v_and_b32_e32 v67, 0xffff0000, v12
	v_lshlrev_b32_e32 v70, 16, v11
	v_and_b32_e32 v71, 0xffff0000, v11
	v_pk_mul_f32 v[68:69], v[64:65], v[64:65]
	v_pk_mul_f32 v[46:47], v[168:169], v[74:75]
	v_pk_mul_f32 v[50:51], v[172:173], v[72:73]
	v_pk_mul_f32 v[48:49], v[170:171], v[76:77]
	v_pk_mul_f32 v[52:53], v[174:175], v[56:57]
	v_pk_mul_f32 v[46:47], v[46:47], v[62:63]
	v_pk_mul_f32 v[50:51], v[50:51], v[58:59]
	v_pk_mul_f32 v[48:49], v[48:49], v[60:61]
	v_pk_mul_f32 v[52:53], v[52:53], v[54:55]
	v_cvt_pk_bf16_f32 v46, v46, v47
	v_cvt_pk_bf16_f32 v47, v48, v49
	v_cvt_pk_bf16_f32 v48, v50, v51
	v_cvt_pk_bf16_f32 v49, v52, v53
	global_store_dwordx4 v121, v[46:49], s[4:5] offset:2048
	v_and_b32_e32 v63, 0xffff0000, v10
	v_and_b32_e32 v53, 0xffff0000, v22
	v_lshlrev_b32_e32 v62, 16, v10
	v_lshlrev_b32_e32 v46, 16, v25
	v_and_b32_e32 v47, 0xffff0000, v25
	v_lshlrev_b32_e32 v48, 16, v24
	v_and_b32_e32 v49, 0xffff0000, v24
	v_lshlrev_b32_e32 v50, 16, v23
	v_and_b32_e32 v51, 0xffff0000, v23
	v_lshlrev_b32_e32 v52, 16, v22
	v_mov_b32_e32 v86, v53
	v_mov_b32_e32 v87, v63
	v_pk_mul_f32 v[72:73], v[66:67], v[66:67]
	v_pk_mul_f32 v[74:75], v[70:71], v[70:71]
	v_pk_mul_f32 v[76:77], v[46:47], v[46:47]
	v_pk_mul_f32 v[78:79], v[48:49], v[48:49]
	v_pk_mul_f32 v[80:81], v[50:51], v[50:51]
	v_mov_b32_e32 v84, v52
	v_mov_b32_e32 v85, v62
	v_pk_mul_f32 v[86:87], v[86:87], v[86:87]
	v_mov_b32_e32 v88, v80
	v_mov_b32_e32 v89, v74
	v_mov_b32_e32 v74, v81
	v_mov_b32_e32 v80, v78
	v_mov_b32_e32 v81, v72
	v_mov_b32_e32 v72, v79
	v_mov_b32_e32 v78, v76
	v_mov_b32_e32 v79, v68
	v_mov_b32_e32 v68, v77
	v_pk_fma_f32 v[76:77], v[84:85], v[84:85], v[86:87]
	v_lshlrev_b32_e32 v84, 16, v33
	v_pk_add_f32 v[76:77], v[88:89], v[76:77]
	v_and_b32_e32 v85, 0xffff0000, v33
	v_pk_add_f32 v[74:75], v[74:75], v[76:77]
	v_lshlrev_b32_e32 v76, 16, v28
	v_pk_add_f32 v[74:75], v[80:81], v[74:75]
	v_and_b32_e32 v77, 0xffff0000, v28
	v_pk_add_f32 v[72:73], v[72:73], v[74:75]
	v_lshlrev_b32_e32 v74, 16, v29
	v_pk_add_f32 v[72:73], v[78:79], v[72:73]
	v_and_b32_e32 v75, 0xffff0000, v29
	v_pk_add_f32 v[68:69], v[68:69], v[72:73]
	ds_bpermute_b32 v73, v1, v69
	ds_bpermute_b32 v72, v1, v68
	v_lshlrev_b32_e32 v78, 16, v27
	v_and_b32_e32 v79, 0xffff0000, v27
	v_lshlrev_b32_e32 v80, 16, v26
	v_and_b32_e32 v81, 0xffff0000, v26
	s_waitcnt lgkmcnt(0)
; DI unsigned pk2(float lo, float hi) { return cvtpk_s(lo, hi); }
; DI void p4_store(const P4Row& R, const float* hg, bf16_t* YC, int row, int lane) {
; #pragma unroll
;     for (int j = 0; j < 4; ++j) {
;         const int c0 = 512 * j + 8 * lane; const u32x4 o = R.o[j], sg = R.sg[j];
;         float v[8] = {bflo(o.x), bfhi(o.x), bflo(o.y), bfhi(o.y), bflo(o.z), bfhi(o.z), bflo(o.w), bfhi(o.w)};
;         const float s[8] = {bflo(sg.x), bfhi(sg.x), bflo(sg.y), bfhi(sg.y), bflo(sg.z), bfhi(sg.z), bflo(sg.w), bfhi(sg.w)};
;         float ss = 0.f;
; #pragma unroll
;         for (int e = 0; e < 8; ++e) ss += v[e] * v[e];
;         ss += __shfl_xor(ss, 1); ss += __shfl_xor(ss, 2); ss += __shfl_xor(ss, 4); ss += __shfl_xor(ss, 8);
;         const float rinv = rsqrtf(ss * (1.0f / 128.0f) + EPS);
;         const f32x4 g0 = *(const f32x4*)(hg + c0), g1 = *(const f32x4*)(hg + c0 + 4);
; #pragma unroll
;         for (int e = 0; e < 4; ++e) { v[e] = v[e] * rinv * g0[e] * s[e]; v[4 + e] = v[4 + e] * rinv * g1[e] * s[4 + e]; }
;         u32x4 w; w.x = pk2(v[0], v[1]); w.y = pk2(v[2], v[3]); w.z = pk2(v[4], v[5]); w.w = pk2(v[6], v[7]);
;         *(u32x4*)(YC + (size_t)row * KCAT + 512 + c0) = w;
;     }
;     {
;         const int c0 = 8 * lane; const float l0 = R.l0, l1 = R.l1, l2 = R.l2; const u32x4 x0 = R.x0, x1 = R.x1, x2 = R.x2;
;         const float mx = fmaxf(l0, fmaxf(l1, l2)); float a0 = __expf(l0 - mx), a1 = __expf(l1 - mx), a2 = __expf(l2 - mx);
;         const float inv = 1.0f / (a0 + a1 + a2); a0 *= inv; a1 *= inv; a2 *= inv;
;         u32x4 w;
;         w.x = pk2(a0 * bflo(x0.x) + a1 * bflo(x1.x) + a2 * bflo(x2.x), a0 * bfhi(x0.x) + a1 * bfhi(x1.x) + a2 * bfhi(x2.x));
;         w.y = pk2(a0 * bflo(x0.y) + a1 * bflo(x1.y) + a2 * bflo(x2.y), a0 * bfhi(x0.y) + a1 * bfhi(x1.y) + a2 * bfhi(x2.y));
;         w.z = pk2(a0 * bflo(x0.z) + a1 * bflo(x1.z) + a2 * bflo(x2.z), a0 * bfhi(x0.z) + a1 * bfhi(x1.z) + a2 * bfhi(x2.z));
;         w.w = pk2(a0 * bflo(x0.w) + a1 * bflo(x1.w) + a2 * bflo(x2.w), a0 * bfhi(x0.w) + a1 * bfhi(x1.w) + a2 * bfhi(x2.w));
;         *(u32x4*)(YC + (size_t)row * KCAT + c0) = w;
;     }
; }
	v_pk_add_f32 v[68:69], v[68:69], v[72:73]
	ds_bpermute_b32 v73, v118, v69
	ds_bpermute_b32 v72, v118, v68
	v_lshlrev_b32_e32 v86, 16, v32
	v_and_b32_e32 v87, 0xffff0000, v32
	s_waitcnt lgkmcnt(0)
	v_pk_add_f32 v[68:69], v[68:69], v[72:73]
	ds_bpermute_b32 v73, v119, v69
	ds_bpermute_b32 v72, v119, v68
	s_waitcnt lgkmcnt(0)
	v_pk_add_f32 v[68:69], v[68:69], v[72:73]
	ds_bpermute_b32 v73, v120, v69
	ds_bpermute_b32 v72, v120, v68
	s_waitcnt lgkmcnt(0)
	v_pk_add_f32 v[68:69], v[68:69], v[72:73]
	s_nop 0
	v_pk_fma_f32 v[68:69], v[68:69], s[20:21], v[82:83] op_sel_hi:[1,0,0]
	v_and_b32_e32 v73, 0xffff0000, v31
	v_mul_f32_e32 v72, 0x4b800000, v69
	v_cmp_gt_f32_e32 vcc, s29, v69
	v_lshlrev_b32_e32 v82, 16, v30
	s_nop 0
	v_cndmask_b32_e32 v69, v69, v72, vcc
	v_rsq_f32_e32 v69, v69
	v_lshlrev_b32_e32 v72, 16, v31
	v_mul_f32_e32 v83, 0x45800000, v69
	v_cndmask_b32_e32 v88, v69, v83, vcc
	v_pk_mul_f32 v[62:63], v[88:89], v[62:63] op_sel_hi:[0,1]
	v_pk_mul_f32 v[66:67], v[88:89], v[66:67] op_sel_hi:[0,1]
	v_pk_mul_f32 v[70:71], v[88:89], v[70:71] op_sel_hi:[0,1]
	v_pk_mul_f32 v[64:65], v[88:89], v[64:65] op_sel_hi:[0,1]
	v_pk_mul_f32 v[58:59], v[180:181], v[62:63]
	v_pk_mul_f32 v[54:55], v[176:177], v[66:67]
	v_pk_mul_f32 v[60:61], v[182:183], v[70:71]
	v_pk_mul_f32 v[56:57], v[178:179], v[64:65]
	v_pk_mul_f32 v[58:59], v[58:59], v[80:81]
	v_pk_mul_f32 v[62:63], v[54:55], v[76:77]
	v_pk_mul_f32 v[60:61], v[60:61], v[78:79]
	v_pk_mul_f32 v[64:65], v[56:57], v[74:75]
	v_cvt_pk_bf16_f32 v54, v58, v59
	v_cvt_pk_bf16_f32 v55, v60, v61
	v_cvt_pk_bf16_f32 v56, v62, v63
	v_cvt_pk_bf16_f32 v57, v64, v65
	global_store_dwordx4 v121, v[54:57], s[4:5] offset:3072
	s_nop 0
	v_max3_f32 v69, v123, v124, v125
	v_sub_f32_e32 v115, v123, v69
	v_sub_f32_e32 v116, v124, v69
	v_sub_f32_e32 v69, v125, v69
	v_mul_f32_e32 v115, 0x3fb8aa3b, v115
	v_mul_f32_e32 v116, 0x3fb8aa3b, v116
	v_mul_f32_e32 v69, 0x3fb8aa3b, v69
	v_exp_f32_e32 v117, v115
	v_exp_f32_e32 v116, v116
	v_exp_f32_e32 v69, v69
	v_lshlrev_b32_e32 v64, 16, v34
	v_and_b32_e32 v65, 0xffff0000, v38
	v_add_f32_e32 v127, v117, v116
	v_add_f32_e32 v128, v69, v127
	v_div_scale_f32 v129, s[24:25], v128, v128, 1.0
	v_rcp_f32_e32 v130, v129
	v_div_scale_f32 v131, vcc, 1.0, v128, 1.0
	v_lshlrev_b32_e32 v62, 16, v38
	v_fma_f32 v132, -v129, v130, 1.0
	v_fmac_f32_e32 v130, v132, v130
	v_mul_f32_e32 v132, v131, v130
	v_fma_f32 v133, -v129, v132, v131
	v_fmac_f32_e32 v132, v133, v130
	v_fma_f32 v129, -v129, v132, v131
	v_div_fmas_f32 v129, v129, v130, v132
	v_div_fixup_f32 v128, v129, v128, 1.0
	v_pk_mul_f32 v[116:117], v[116:117], v[128:129] op_sel_hi:[1,0]
	v_and_b32_e32 v63, 0xffff0000, v34
	v_pk_mul_f32 v[64:65], v[116:117], v[64:65] op_sel:[1,0] op_sel_hi:[0,1]
	v_lshlrev_b32_e32 v66, 16, v42
	v_and_b32_e32 v67, 0xffff0000, v42
	v_mul_f32_e32 v130, v69, v128
	v_pk_fma_f32 v[62:63], v[116:117], v[62:63], v[64:65]
	v_cmp_gt_f32_e32 vcc, s29, v68
	v_pk_fma_f32 v[62:63], v[130:131], v[66:67], v[62:63] op_sel_hi:[0,1,1]
	v_cvt_pk_bf16_f32 v62, v62, v63
	v_mul_f32_e32 v63, 0x4b800000, v68
	v_cndmask_b32_e32 v63, v68, v63, vcc
	v_lshlrev_b32_e32 v74, 16, v35
	v_and_b32_e32 v75, 0xffff0000, v39
	v_lshlrev_b32_e32 v80, 16, v36
	v_and_b32_e32 v81, 0xffff0000, v40
	v_rsq_f32_e32 v68, v63
	v_lshlrev_b32_e32 v70, 16, v39
	v_and_b32_e32 v71, 0xffff0000, v35
	v_lshlrev_b32_e32 v78, 16, v40
	v_and_b32_e32 v79, 0xffff0000, v36
	v_pk_mul_f32 v[74:75], v[116:117], v[74:75] op_sel:[1,0] op_sel_hi:[0,1]
	v_pk_mul_f32 v[80:81], v[116:117], v[80:81] op_sel:[1,0] op_sel_hi:[0,1]
	v_lshlrev_b32_e32 v76, 16, v43
	v_and_b32_e32 v77, 0xffff0000, v43
	v_lshlrev_b32_e32 v88, 16, v44
	v_and_b32_e32 v89, 0xffff0000, v44
	v_pk_fma_f32 v[64:65], v[116:117], v[70:71], v[74:75]
	v_pk_fma_f32 v[70:71], v[116:117], v[78:79], v[80:81]
	v_pk_fma_f32 v[64:65], v[130:131], v[76:77], v[64:65] op_sel_hi:[0,1,1]
	v_pk_fma_f32 v[66:67], v[130:131], v[88:89], v[70:71] op_sel_hi:[0,1,1]
	v_cvt_pk_bf16_f32 v63, v64, v65
	v_cvt_pk_bf16_f32 v64, v66, v67
	v_mul_f32_e32 v66, 0x45800000, v68
	v_cndmask_b32_e32 v66, v68, v66, vcc
	v_and_b32_e32 v115, 0xffff0000, v41
	v_pk_mul_f32 v[52:53], v[66:67], v[52:53] op_sel_hi:[0,1]
	v_pk_mul_f32 v[48:49], v[66:67], v[48:49] op_sel_hi:[0,1]
	v_pk_mul_f32 v[50:51], v[66:67], v[50:51] op_sel_hi:[0,1]
	v_pk_mul_f32 v[46:47], v[66:67], v[46:47] op_sel_hi:[0,1]
	v_and_b32_e32 v83, 0xffff0000, v30
	v_pk_mul_f32 v[114:115], v[116:117], v[114:115] op_sel:[1,0] op_sel_hi:[0,1]
	v_and_b32_e32 v127, 0xffff0000, v45
	v_pk_fma_f32 v[74:75], v[116:117], v[112:113], v[114:115]
	v_pk_mul_f32 v[48:49], v[184:185], v[48:49]
	v_pk_mul_f32 v[52:53], v[188:189], v[52:53]
	v_pk_mul_f32 v[50:51], v[190:191], v[50:51]
	v_pk_mul_f32 v[46:47], v[186:187], v[46:47]
	v_pk_mul_f32 v[52:53], v[52:53], v[82:83]
	v_pk_mul_f32 v[48:49], v[48:49], v[86:87]
	v_pk_mul_f32 v[50:51], v[50:51], v[72:73]
	v_pk_mul_f32 v[54:55], v[46:47], v[84:85]
	v_pk_fma_f32 v[70:71], v[130:131], v[126:127], v[74:75] op_sel_hi:[0,1,1]
	v_cvt_pk_bf16_f32 v46, v52, v53
	v_cvt_pk_bf16_f32 v47, v50, v51
	v_cvt_pk_bf16_f32 v48, v48, v49
	v_cvt_pk_bf16_f32 v49, v54, v55
	v_cvt_pk_bf16_f32 v65, v70, v71
	global_store_dwordx4 v122, v[46:49], s[4:5] offset:1024
	global_store_dwordx4 v121, v[62:65], s[4:5]
	s_branch .LBB0_527
